# phase-0 adaLN GEMV loop unrolled x2: 32 weight loads in flight per wave before the first FMA (was 16), same FMA order
# speedup vs baseline: 1.0085x; 1.0006x over previous
.LBB0_23:
	v_subrev_u32_e32 v17, 30, v16
	v_subrev_u32_e32 v30, 28, v16
	v_subrev_u32_e32 v32, 26, v16
	v_subrev_u32_e32 v34, 24, v16
	v_subrev_u32_e32 v36, 22, v16
	v_subrev_u32_e32 v38, 20, v16
	v_subrev_u32_e32 v40, 18, v16
	v_add_u32_e32 v42, -16, v16
	v_add_u32_e32 v44, -14, v16
	v_add_u32_e32 v46, -12, v16
	v_add_u32_e32 v48, -10, v16
	v_add_u32_e32 v50, -8, v16
	v_add_u32_e32 v52, -6, v16
	v_add_u32_e32 v54, -4, v16
	v_add_u32_e32 v56, -2, v16
	v_mad_i64_i32 v[18:19], s[16:17], v16, s12, v[4:5]
	v_mad_i64_i32 v[28:29], s[16:17], v17, s12, v[4:5]
	v_mad_i64_i32 v[30:31], s[16:17], v30, s12, v[4:5]
	v_mad_i64_i32 v[32:33], s[16:17], v32, s12, v[4:5]
	v_mad_i64_i32 v[34:35], s[16:17], v34, s12, v[4:5]
	v_mad_i64_i32 v[36:37], s[16:17], v36, s12, v[4:5]
	v_mad_i64_i32 v[38:39], s[16:17], v38, s12, v[4:5]
	v_mad_i64_i32 v[40:41], s[16:17], v40, s12, v[4:5]
	v_mad_i64_i32 v[42:43], s[16:17], v42, s12, v[4:5]
	v_mad_i64_i32 v[44:45], s[16:17], v44, s12, v[4:5]
	v_mad_i64_i32 v[46:47], s[16:17], v46, s12, v[4:5]
	v_mad_i64_i32 v[48:49], s[16:17], v48, s12, v[4:5]
	v_mad_i64_i32 v[50:51], s[16:17], v50, s12, v[4:5]
	v_mad_i64_i32 v[52:53], s[16:17], v52, s12, v[4:5]
	v_mad_i64_i32 v[54:55], s[16:17], v54, s12, v[4:5]
	v_mad_i64_i32 v[56:57], s[16:17], v56, s12, v[4:5]
	v_add_u32_e32 v134, 2, v16
	v_mad_i64_i32 v[136:137], s[16:17], v134, s12, v[4:5]
	v_add_u32_e32 v138, 4, v16
	v_mad_i64_i32 v[140:141], s[16:17], v138, s12, v[4:5]
	v_add_u32_e32 v142, 6, v16
	v_mad_i64_i32 v[144:145], s[16:17], v142, s12, v[4:5]
	v_add_u32_e32 v146, 8, v16
	v_mad_i64_i32 v[148:149], s[16:17], v146, s12, v[4:5]
	v_add_u32_e32 v150, 10, v16
	v_mad_i64_i32 v[152:153], s[16:17], v150, s12, v[4:5]
	v_add_u32_e32 v154, 12, v16
	v_mad_i64_i32 v[156:157], s[16:17], v154, s12, v[4:5]
	v_add_u32_e32 v158, 14, v16
	v_mad_i64_i32 v[160:161], s[16:17], v158, s12, v[4:5]
	v_add_u32_e32 v162, 16, v16
	v_mad_i64_i32 v[164:165], s[16:17], v162, s12, v[4:5]
	v_add_u32_e32 v166, 18, v16
	v_mad_i64_i32 v[168:169], s[16:17], v166, s12, v[4:5]
	v_add_u32_e32 v170, 20, v16
	v_mad_i64_i32 v[172:173], s[16:17], v170, s12, v[4:5]
	v_add_u32_e32 v174, 22, v16
	v_mad_i64_i32 v[176:177], s[16:17], v174, s12, v[4:5]
	v_add_u32_e32 v178, 24, v16
	v_mad_i64_i32 v[180:181], s[16:17], v178, s12, v[4:5]
	v_add_u32_e32 v182, 26, v16
	v_mad_i64_i32 v[184:185], s[16:17], v182, s12, v[4:5]
	v_add_u32_e32 v186, 28, v16
	v_mad_i64_i32 v[188:189], s[16:17], v186, s12, v[4:5]
	v_add_u32_e32 v190, 30, v16
	v_mad_i64_i32 v[192:193], s[16:17], v190, s12, v[4:5]
	v_add_u32_e32 v194, 32, v16
	v_mad_i64_i32 v[196:197], s[16:17], v194, s12, v[4:5]
	global_load_dword v58, v[28:29], off nt
	global_load_dword v60, v[30:31], off nt
	global_load_dword v62, v[32:33], off nt
	global_load_dword v64, v[34:35], off nt
	global_load_dword v66, v[36:37], off nt
	global_load_dword v68, v[38:39], off nt
	global_load_dword v70, v[40:41], off nt
	global_load_dword v72, v[42:43], off nt
	global_load_dword v76, v[44:45], off nt
	global_load_dword v78, v[46:47], off nt
	global_load_dword v80, v[48:49], off nt
	global_load_dword v82, v[50:51], off nt
	global_load_dword v84, v[52:53], off nt
	global_load_dword v86, v[54:55], off nt
	global_load_dword v88, v[56:57], off nt
	s_nop 0
	global_load_dword v18, v[18:19], off nt
	global_load_dword v102, v[136:137], off nt
	global_load_dword v104, v[140:141], off nt
	global_load_dword v106, v[144:145], off nt
	global_load_dword v108, v[148:149], off nt
	global_load_dword v110, v[152:153], off nt
	global_load_dword v112, v[156:157], off nt
	global_load_dword v114, v[160:161], off nt
	global_load_dword v116, v[164:165], off nt
	global_load_dword v118, v[168:169], off nt
	global_load_dword v120, v[172:173], off nt
	global_load_dword v122, v[176:177], off nt
	global_load_dword v124, v[180:181], off nt
	global_load_dword v126, v[184:185], off nt
	global_load_dword v128, v[188:189], off nt
	global_load_dword v130, v[192:193], off nt
	global_load_dword v132, v[196:197], off nt
	ds_read2_b32 v[20:21], v15 offset1:2
	ds_read2_b32 v[22:23], v15 offset0:4 offset1:6
	ds_read2_b32 v[24:25], v15 offset0:8 offset1:10
	ds_read2_b32 v[26:27], v15 offset0:12 offset1:14
	v_add_u32_e32 v59, 0x2000, v15
	v_add_u32_e32 v61, 0x4000, v15
	ds_read2_b32 v[28:29], v15 offset0:16 offset1:18
	ds_read2_b32 v[30:31], v15 offset0:20 offset1:22
	ds_read2_b32 v[32:33], v15 offset0:24 offset1:26
	ds_read2_b32 v[34:35], v15 offset0:28 offset1:30
	ds_read2_b32 v[36:37], v59 offset1:2
	ds_read2_b32 v[38:39], v61 offset1:2
	ds_read2_b32 v[40:41], v59 offset0:4 offset1:6
	ds_read2_b32 v[42:43], v61 offset0:4 offset1:6
	ds_read2_b32 v[44:45], v59 offset0:8 offset1:10
	ds_read2_b32 v[46:47], v61 offset0:8 offset1:10
	ds_read2_b32 v[48:49], v59 offset0:12 offset1:14
	ds_read2_b32 v[50:51], v61 offset0:12 offset1:14
	ds_read2_b32 v[52:53], v59 offset0:16 offset1:18
	ds_read2_b32 v[54:55], v61 offset0:16 offset1:18
	ds_read2_b32 v[56:57], v59 offset0:20 offset1:22
	ds_read2_b32 v[90:91], v61 offset0:20 offset1:22
	ds_read2_b32 v[92:93], v59 offset0:24 offset1:26
	ds_read2_b32 v[94:95], v61 offset0:24 offset1:26
	ds_read2_b32 v[96:97], v59 offset0:28 offset1:30
	ds_read2_b32 v[98:99], v61 offset0:28 offset1:30
	s_waitcnt lgkmcnt(14)
	v_mov_b32_e32 v100, v20
	v_mov_b32_e32 v101, v36
	v_mov_b32_e32 v36, v21
	v_mov_b32_e32 v20, v22
	s_waitcnt lgkmcnt(13)
	v_mov_b32_e32 v21, v40
	v_mov_b32_e32 v40, v23
	v_mov_b32_e32 v22, v24
	s_waitcnt lgkmcnt(11)
	v_mov_b32_e32 v23, v44
	v_mov_b32_e32 v44, v25
	v_mov_b32_e32 v24, v26
	s_waitcnt lgkmcnt(9)
	v_mov_b32_e32 v25, v48
	v_mov_b32_e32 v48, v27
	v_mov_b32_e32 v26, v28
	s_waitcnt lgkmcnt(7)
	v_mov_b32_e32 v27, v52
	v_mov_b32_e32 v52, v29
	v_mov_b32_e32 v28, v30
	s_waitcnt lgkmcnt(5)
	v_mov_b32_e32 v29, v56
	v_mov_b32_e32 v56, v31
	v_mov_b32_e32 v30, v32
	s_waitcnt lgkmcnt(3)
	v_mov_b32_e32 v31, v92
	v_mov_b32_e32 v92, v33
	v_mov_b32_e32 v32, v34
	s_waitcnt lgkmcnt(1)
	v_mov_b32_e32 v33, v96
	v_mov_b32_e32 v96, v35
	s_waitcnt vmcnt(31)
	v_pk_fma_f32 v[6:7], v[58:59], v[100:101], v[6:7] op_sel_hi:[0,1,1]
	v_fmac_f32_e32 v14, v58, v38
	s_waitcnt vmcnt(30)
	v_fmac_f32_e32 v14, v60, v39
	v_pk_fma_f32 v[6:7], v[60:61], v[36:37], v[6:7] op_sel_hi:[0,1,1]
	s_waitcnt vmcnt(29)
	v_pk_fma_f32 v[6:7], v[62:63], v[20:21], v[6:7] op_sel_hi:[0,1,1]
	v_fmac_f32_e32 v14, v62, v42
	s_waitcnt vmcnt(28)
	v_fmac_f32_e32 v14, v64, v43
	v_pk_fma_f32 v[6:7], v[64:65], v[40:41], v[6:7] op_sel_hi:[0,1,1]
	s_waitcnt vmcnt(27)
	v_pk_fma_f32 v[6:7], v[66:67], v[22:23], v[6:7] op_sel_hi:[0,1,1]
	v_fmac_f32_e32 v14, v66, v46
	s_waitcnt vmcnt(26)
	v_fmac_f32_e32 v14, v68, v47
	v_pk_fma_f32 v[6:7], v[68:69], v[44:45], v[6:7] op_sel_hi:[0,1,1]
	s_waitcnt vmcnt(25)
	v_fmac_f32_e32 v14, v70, v50
	v_pk_fma_f32 v[6:7], v[70:71], v[24:25], v[6:7] op_sel_hi:[0,1,1]
	s_waitcnt vmcnt(24)
	v_fmac_f32_e32 v14, v72, v51
	v_pk_fma_f32 v[6:7], v[72:73], v[48:49], v[6:7] op_sel_hi:[0,1,1]
	s_waitcnt vmcnt(23)
	v_fmac_f32_e32 v14, v76, v54
	v_pk_fma_f32 v[6:7], v[76:77], v[26:27], v[6:7] op_sel_hi:[0,1,1]
	s_waitcnt vmcnt(22)
	v_fmac_f32_e32 v14, v78, v55
	v_pk_fma_f32 v[6:7], v[78:79], v[52:53], v[6:7] op_sel_hi:[0,1,1]
	s_waitcnt vmcnt(21)
	v_fmac_f32_e32 v14, v80, v90
	v_pk_fma_f32 v[6:7], v[80:81], v[28:29], v[6:7] op_sel_hi:[0,1,1]
	s_waitcnt vmcnt(20)
	v_fmac_f32_e32 v14, v82, v91
	v_pk_fma_f32 v[6:7], v[82:83], v[56:57], v[6:7] op_sel_hi:[0,1,1]
	s_waitcnt vmcnt(19)
	v_fmac_f32_e32 v14, v84, v94
	v_pk_fma_f32 v[6:7], v[84:85], v[30:31], v[6:7] op_sel_hi:[0,1,1]
	s_waitcnt vmcnt(18)
	v_fmac_f32_e32 v14, v86, v95
	v_pk_fma_f32 v[6:7], v[86:87], v[92:93], v[6:7] op_sel_hi:[0,1,1]
	s_waitcnt vmcnt(17)
	v_pk_fma_f32 v[6:7], v[88:89], v[32:33], v[6:7] op_sel_hi:[0,1,1]
	s_waitcnt lgkmcnt(0)
	v_fmac_f32_e32 v14, v88, v98
	s_waitcnt vmcnt(16)
	v_pk_fma_f32 v[6:7], v[18:19], v[96:97], v[6:7] op_sel_hi:[0,1,1]
	v_fmac_f32_e32 v14, v18, v99
	ds_read2_b32 v[20:21], v15 offset0:32 offset1:34
	ds_read2_b32 v[22:23], v15 offset0:36 offset1:38
	ds_read2_b32 v[24:25], v15 offset0:40 offset1:42
	ds_read2_b32 v[26:27], v15 offset0:44 offset1:46
	ds_read2_b32 v[28:29], v15 offset0:48 offset1:50
	ds_read2_b32 v[30:31], v15 offset0:52 offset1:54
	ds_read2_b32 v[32:33], v15 offset0:56 offset1:58
	ds_read2_b32 v[34:35], v15 offset0:60 offset1:62
	ds_read2_b32 v[36:37], v59 offset0:32 offset1:34
	ds_read2_b32 v[38:39], v61 offset0:32 offset1:34
	ds_read2_b32 v[40:41], v59 offset0:36 offset1:38
	ds_read2_b32 v[42:43], v61 offset0:36 offset1:38
	ds_read2_b32 v[44:45], v59 offset0:40 offset1:42
	ds_read2_b32 v[46:47], v61 offset0:40 offset1:42
	ds_read2_b32 v[48:49], v59 offset0:44 offset1:46
	ds_read2_b32 v[50:51], v61 offset0:44 offset1:46
	ds_read2_b32 v[52:53], v59 offset0:48 offset1:50
	ds_read2_b32 v[54:55], v61 offset0:48 offset1:50
	ds_read2_b32 v[56:57], v59 offset0:52 offset1:54
	ds_read2_b32 v[90:91], v61 offset0:52 offset1:54
	ds_read2_b32 v[92:93], v59 offset0:56 offset1:58
	ds_read2_b32 v[94:95], v61 offset0:56 offset1:58
	ds_read2_b32 v[96:97], v59 offset0:60 offset1:62
	ds_read2_b32 v[98:99], v61 offset0:60 offset1:62
	s_waitcnt lgkmcnt(14)
	v_mov_b32_e32 v100, v20
	v_mov_b32_e32 v101, v36
	v_mov_b32_e32 v36, v21
	v_mov_b32_e32 v20, v22
	s_waitcnt lgkmcnt(13)
	v_mov_b32_e32 v21, v40
	v_mov_b32_e32 v40, v23
	v_mov_b32_e32 v22, v24
	s_waitcnt lgkmcnt(11)
	v_mov_b32_e32 v23, v44
	v_mov_b32_e32 v44, v25
	v_mov_b32_e32 v24, v26
	s_waitcnt lgkmcnt(9)
	v_mov_b32_e32 v25, v48
	v_mov_b32_e32 v48, v27
	v_mov_b32_e32 v26, v28
	s_waitcnt lgkmcnt(7)
	v_mov_b32_e32 v27, v52
	v_mov_b32_e32 v52, v29
	v_mov_b32_e32 v28, v30
	s_waitcnt lgkmcnt(5)
	v_mov_b32_e32 v29, v56
	v_mov_b32_e32 v56, v31
	v_mov_b32_e32 v30, v32
	s_waitcnt lgkmcnt(3)
	v_mov_b32_e32 v31, v92
	v_mov_b32_e32 v92, v33
	v_mov_b32_e32 v32, v34
	s_waitcnt lgkmcnt(1)
	v_mov_b32_e32 v33, v96
	v_mov_b32_e32 v96, v35
	s_waitcnt vmcnt(15)
	v_pk_fma_f32 v[6:7], v[102:103], v[100:101], v[6:7] op_sel_hi:[0,1,1]
	v_fmac_f32_e32 v14, v102, v38
	s_waitcnt vmcnt(14)
	v_fmac_f32_e32 v14, v104, v39
	v_pk_fma_f32 v[6:7], v[104:105], v[36:37], v[6:7] op_sel_hi:[0,1,1]
	s_waitcnt vmcnt(13)
	v_pk_fma_f32 v[6:7], v[106:107], v[20:21], v[6:7] op_sel_hi:[0,1,1]
	v_fmac_f32_e32 v14, v106, v42
	s_waitcnt vmcnt(12)
	v_fmac_f32_e32 v14, v108, v43
	v_pk_fma_f32 v[6:7], v[108:109], v[40:41], v[6:7] op_sel_hi:[0,1,1]
	s_waitcnt vmcnt(11)
	v_pk_fma_f32 v[6:7], v[110:111], v[22:23], v[6:7] op_sel_hi:[0,1,1]
	v_fmac_f32_e32 v14, v110, v46
	s_waitcnt vmcnt(10)
	v_fmac_f32_e32 v14, v112, v47
	v_pk_fma_f32 v[6:7], v[112:113], v[44:45], v[6:7] op_sel_hi:[0,1,1]
	s_waitcnt vmcnt(9)
	v_fmac_f32_e32 v14, v114, v50
	v_pk_fma_f32 v[6:7], v[114:115], v[24:25], v[6:7] op_sel_hi:[0,1,1]
	s_waitcnt vmcnt(8)
	v_fmac_f32_e32 v14, v116, v51
	v_pk_fma_f32 v[6:7], v[116:117], v[48:49], v[6:7] op_sel_hi:[0,1,1]
	s_waitcnt vmcnt(7)
	v_fmac_f32_e32 v14, v118, v54
	v_pk_fma_f32 v[6:7], v[118:119], v[26:27], v[6:7] op_sel_hi:[0,1,1]
	s_waitcnt vmcnt(6)
	v_fmac_f32_e32 v14, v120, v55
	v_pk_fma_f32 v[6:7], v[120:121], v[52:53], v[6:7] op_sel_hi:[0,1,1]
	s_waitcnt vmcnt(5)
	v_fmac_f32_e32 v14, v122, v90
	v_pk_fma_f32 v[6:7], v[122:123], v[28:29], v[6:7] op_sel_hi:[0,1,1]
	s_waitcnt vmcnt(4)
	v_fmac_f32_e32 v14, v124, v91
	v_pk_fma_f32 v[6:7], v[124:125], v[56:57], v[6:7] op_sel_hi:[0,1,1]
	s_waitcnt vmcnt(3)
	v_fmac_f32_e32 v14, v126, v94
	v_pk_fma_f32 v[6:7], v[126:127], v[30:31], v[6:7] op_sel_hi:[0,1,1]
	s_waitcnt vmcnt(2)
	v_fmac_f32_e32 v14, v128, v95
	v_pk_fma_f32 v[6:7], v[128:129], v[92:93], v[6:7] op_sel_hi:[0,1,1]
	s_waitcnt vmcnt(1)
	v_pk_fma_f32 v[6:7], v[130:131], v[32:33], v[6:7] op_sel_hi:[0,1,1]
	s_waitcnt lgkmcnt(0)
	v_fmac_f32_e32 v14, v130, v98
	s_waitcnt vmcnt(0)
	v_pk_fma_f32 v[6:7], v[132:133], v[96:97], v[6:7] op_sel_hi:[0,1,1]
	v_fmac_f32_e32 v14, v132, v99
	s_add_i32 s8, s8, 32
	v_add_u32_e32 v16, 64, v16
	v_add_u32_e32 v15, 0x100, v15
	s_cmpk_lt_u32 s8, 0x70
	s_cbranch_scc1 .LBB0_23
	ds_write2st64_b32 v8, v6, v7 offset0:128 offset1:136
	ds_write_b32 v8, v14 offset:36864
	s_waitcnt lgkmcnt(0)
	s_barrier
	s_and_saveexec_b64 s[8:9], vcc
	s_cbranch_execz .LBB0_21
	s_mul_i32 s16, s5, 0x3000
	s_add_i32 s16, s16, s4
	v_add_u32_e32 v4, s16, v2
	v_ashrrev_i32_e32 v5, 31, v4
	v_lshl_add_u64 v[4:5], v[4:5], 2, s[0:1]
	global_load_dword v28, v[4:5], off
	v_add_u32_e32 v18, 0x8000, v9
	v_add_u32_e32 v26, 0x8400, v9
	ds_read2_b32 v[6:7], v18 offset1:32
	ds_read2_b32 v[14:15], v18 offset0:64 offset1:96
	ds_read2_b32 v[16:17], v18 offset0:128 offset1:160
	ds_read2_b32 v[18:19], v18 offset0:192 offset1:224
	ds_read2_b32 v[20:21], v26 offset1:32
	ds_read2_b32 v[22:23], v26 offset0:64 offset1:96
	ds_read2_b32 v[24:25], v26 offset0:128 offset1:160
	ds_read2_b32 v[26:27], v26 offset0:192 offset1:224
	s_waitcnt lgkmcnt(7)
	v_add_f32_e32 v6, 0, v6
	v_add_f32_e32 v6, v6, v7
	s_waitcnt lgkmcnt(6)
	v_add_f32_e32 v6, v6, v14
	v_add_f32_e32 v6, v6, v15
	s_waitcnt lgkmcnt(5)
	v_add_f32_e32 v6, v6, v16
	v_add_f32_e32 v6, v6, v17
	s_waitcnt lgkmcnt(4)
	v_add_f32_e32 v6, v6, v18
	v_add_f32_e32 v6, v6, v19
	s_waitcnt lgkmcnt(3)
	v_add_f32_e32 v6, v6, v20
	v_add_f32_e32 v6, v6, v21
	v_mad_u64_u32 v[4:5], s[16:17], s5, 3, v[0:1]
	s_waitcnt lgkmcnt(2)
	v_add_f32_e32 v6, v6, v22
	v_mul_lo_u32 v4, v4, 6
	v_add_f32_e32 v6, v6, v23
	v_ashrrev_i32_e32 v5, 31, v4
	s_waitcnt lgkmcnt(1)
	v_add_f32_e32 v6, v6, v24
	v_lshlrev_b64 v[4:5], 13, v[4:5]
	v_add_f32_e32 v6, v6, v25
	s_ashr_i32 s5, s4, 31
	v_lshl_add_u64 v[4:5], s[2:3], 0, v[4:5]
	s_waitcnt lgkmcnt(0)
	v_add_f32_e32 v6, v6, v26
	v_lshl_add_u64 v[4:5], s[4:5], 2, v[4:5]
	v_add_f32_e32 v6, v6, v27
	v_lshl_add_u64 v[4:5], v[2:3], 2, v[4:5]
	s_waitcnt vmcnt(0)
	v_add_f32_e32 v6, v6, v28
	global_store_dword v[4:5], v6, off
	s_branch .LBB0_21
